# P1+P7 row loops: param loads hoisted (P7 via LDS-parked products), P10 tile lookup via scalar loads issued a unit ahead
# speedup vs baseline: 1.0328x; 1.0328x over previous
; __device__ __forceinline__ void phase1(const Args& a, int lane, int wave, int vcu, int G) {
;     ...
;     for (int m = vcu * 8 + wave; m < MROWS; m += G * 8) {
;         const float* xr = m < NT ? a.in[0] + (size_t)m * 2048 : a.in[2] + (size_t)(m - NT) * 2048;
;         const float* mr = mod + (size_t)(m < NT ? (m >> 11) : 8) * 12288;
;         f32x4 v[8]; float ss = 0.f;
; #pragma unroll
;         for (int j = 0; j < 8; ++j) { v[j] = __builtin_nontemporal_load((const f32x4*)(xr + 4 * (lane + 64 * j))); ss += v[j][0] * v[j][0] + v[j][1] * v[j][1] + v[j][2] * v[j][2] + v[j][3] * v[j][3]; }
;         const float rstd = rsqrtf(wave_sum(ss) * (1.f / 2048.f) + EPS);
.LBB0_87:
	s_cmp_gt_i32 s94, 1
	s_cselect_b64 s[0:1], -1, 0
	s_cmp_lt_i32 s95, 2
	s_cselect_b64 s[2:3], -1, 0
	s_or_b64 s[0:1], s[0:1], s[2:3]
	s_and_b64 vcc, exec, s[0:1]
	s_cbranch_vccnz .LBB0_143
	v_mov_b32_e32 v1, v0
	s_nop 0
	v_readfirstlane_b32 s0, v1
	s_ashr_i32 s1, s0, 6
	v_readlane_b32 s0, v246, 2
	s_lshl_b32 s2, s0, 3
	s_add_i32 s0, s1, s2
	s_cmpk_gt_i32 s0, 0x47ff
	s_cbranch_scc1 .LBB0_93
	v_lshlrev_b32_e32 v1, 2, v1
	v_and_b32_e32 v2, 0xfc, v1
	v_mov_b32_e32 v5, 0
	v_lshlrev_b32_e32 v4, 2, v2
	v_or_b32_e32 v12, 0x400, v2
	s_waitcnt lgkmcnt(0)
	v_lshl_add_u64 v[26:27], s[80:81], 0, v[4:5]
	v_or_b32_e32 v14, 0x500, v2
	v_lshlrev_b32_e32 v4, 2, v12
	v_or_b32_e32 v16, 0x600, v2
	v_lshl_add_u64 v[28:29], s[80:81], 0, v[4:5]
	v_lshlrev_b32_e32 v4, 2, v14
	v_or_b32_e32 v18, 0x700, v2
	v_lshl_add_u64 v[30:31], s[80:81], 0, v[4:5]
	v_lshlrev_b32_e32 v4, 2, v16
	v_lshl_add_u64 v[32:33], s[80:81], 0, v[4:5]
	v_lshlrev_b32_e32 v4, 2, v18
	v_lshl_add_u64 v[34:35], s[80:81], 0, v[4:5]
	v_lshlrev_b32_e32 v4, 1, v2
	s_add_u32 s16, s92, 0x100000
	v_lshl_add_u64 v[4:5], s[92:93], 0, v[4:5]
	s_mov_b64 s[4:5], 0x1a200000
	s_addc_u32 s17, s93, 0
	s_lshl_b32 s0, s97, 3
	v_lshl_add_u64 v[36:37], v[4:5], 0, s[4:5]
	s_ashr_i32 s3, s1, 31
	s_ashr_i32 s5, s2, 31
	s_add_u32 s4, s1, s2
	s_addc_u32 s5, s3, s5
	s_ashr_i32 s1, s0, 31
	s_lshl_b64 s[2:3], s[4:5], 13
	v_or_b32_e32 v6, 0x100, v2
	v_or_b32_e32 v8, 0x200, v2
	v_or_b32_e32 v10, 0x300, v2
	s_add_u32 s6, s68, s2
	s_addc_u32 s7, s69, s3
	s_lshl_b64 s[8:9], s[0:1], 13
	s_mov_b32 s11, 0
	v_lshlrev_b32_e32 v1, 2, v2
	v_lshlrev_b32_e32 v41, 2, v12
	v_lshlrev_b32_e32 v42, 2, v14
	v_lshlrev_b32_e32 v43, 2, v16
	v_lshlrev_b32_e32 v44, 2, v18
	v_mov_b32_e32 v45, 0x358637bd
	v_mov_b32_e32 v46, 0x3a000000
	s_mov_b32 s18, 0x800000
	s_movk_i32 s19, 0x7fff
	s_mov_b32 s20, 0xffff0000
	v_lshlrev_b32_e32 v47, 2, v6
	v_lshlrev_b32_e32 v48, 2, v8
	v_lshlrev_b32_e32 v49, 2, v10
	global_load_dwordx4 v[90:93], v[26:27], off
	global_load_dwordx4 v[94:97], v[26:27], off offset:1024
	global_load_dwordx4 v[98:101], v[26:27], off offset:2048
	global_load_dwordx4 v[102:105], v[26:27], off offset:3072
	global_load_dwordx4 v[106:109], v[28:29], off
	global_load_dwordx4 v[110:113], v[30:31], off
	global_load_dwordx4 v[114:117], v[32:33], off
	global_load_dwordx4 v[118:121], v[34:35], off
	s_branch .LBB0_91
.LBB0_90:
	global_load_dwordx4 v[50:53], v1, s[12:13] nt
	global_load_dwordx4 v[54:57], v1, s[12:13] offset:1024 nt
	global_load_dwordx4 v[22:25], v1, s[12:13] offset:2048 nt
	global_load_dwordx4 v[18:21], v1, s[12:13] offset:3072 nt
	global_load_dwordx4 v[14:17], v41, s[12:13] nt
	global_load_dwordx4 v[10:13], v42, s[12:13] nt
	global_load_dwordx4 v[6:9], v43, s[12:13] nt
	global_load_dwordx4 v[2:5], v44, s[12:13] nt
	s_min_i32 s10, s4, 0x4000
	s_ashr_i32 s10, s10, 11
	s_mul_hi_i32 s13, s10, 0xc000
	s_mul_i32 s10, s10, 0xc000
	s_add_u32 s12, s16, s10
	s_addc_u32 s13, s17, s13
	s_add_u32 s14, s12, 0x2000
	s_addc_u32 s15, s13, 0
	global_load_dwordx4 v[122:125], v1, s[14:15]
	global_load_dwordx4 v[126:129], v1, s[14:15] offset:1024
	global_load_dwordx4 v[130:133], v1, s[14:15] offset:2048
	global_load_dwordx4 v[134:137], v1, s[14:15] offset:3072
	global_load_dwordx4 v[138:141], v41, s[14:15]
	global_load_dwordx4 v[142:145], v42, s[14:15]
	global_load_dwordx4 v[146:149], v43, s[14:15]
	global_load_dwordx4 v[150:153], v44, s[14:15]
	global_load_dwordx4 v[154:157], v1, s[12:13]
	global_load_dwordx4 v[158:161], v1, s[12:13] offset:1024
	global_load_dwordx4 v[162:165], v1, s[12:13] offset:2048
	global_load_dwordx4 v[166:169], v1, s[12:13] offset:3072
	global_load_dwordx4 v[170:173], v41, s[12:13]
	global_load_dwordx4 v[174:177], v42, s[12:13]
	global_load_dwordx4 v[178:181], v43, s[12:13]
	global_load_dwordx4 v[182:185], v44, s[12:13]
	v_mov_b32_e32 v40, 0
	v_mov_b32_e32 v84, 0
	s_lshl_b64 s[2:3], s[2:3], 12
	s_add_u32 s4, s4, s0
	s_addc_u32 s5, s5, s1
	s_add_u32 s6, s6, s8
	s_addc_u32 s7, s7, s9
	s_cmpk_lt_i32 s4, 0x4800
	s_waitcnt vmcnt(16)
; __device__ __forceinline__ unsigned pk2(float lo, float hi) { return f2bf(lo) | (f2bf(hi) << 16); }
; __device__ __forceinline__ float wave_sum(float v) {
;     v += dppf<0x111, 0xf, true>(v); v += dppf<0x112, 0xf, true>(v); v += dppf<0x114, 0xf, true>(v); v += dppf<0x118, 0xf, true>(v);
;     v += dppf<0x142, 0xa>(v); v += dppf<0x143, 0xc>(v);
;     return __builtin_bit_cast(float, __builtin_amdgcn_readlane(__builtin_bit_cast(int, v), 63));
; }
; __device__ __forceinline__ void phase1(const Args& a, int lane, int wave, int vcu, int G) {
;     ...
;         for (int j = 0; j < 8; ++j) { v[j] = __builtin_nontemporal_load((const f32x4*)(xr + 4 * (lane + 64 * j))); ss += v[j][0] * v[j][0] + v[j][1] * v[j][1] + v[j][2] * v[j][2] + v[j][3] * v[j][3]; }
;         const float rstd = rsqrtf(wave_sum(ss) * (1.f / 2048.f) + EPS);
; #pragma unroll
;         for (int j = 0; j < 8; ++j) { const int c = 4 * (lane + 64 * j); const f32x4 gg = *(const f32x4*)(g + c), sh = *(const f32x4*)(mr + c), sc = *(const f32x4*)(mr + 2048 + c);
;             const f32x4 o = v[j] * rstd * gg * (sc + 1.f) + sh;
;             v2u q; q.x = pk2(o[0], o[1]); q.y = pk2(o[2], o[3]); *(v2u*)(H + (size_t)m * 2048 + c) = q; }
;     }
	v_mul_f32_e32 v85, v50, v50
	v_mul_f32_e32 v86, v54, v54
	v_mul_f32_e32 v87, v22, v22
	v_mul_f32_e32 v88, v18, v18
	v_fmac_f32_e32 v85, v51, v51
	v_fmac_f32_e32 v86, v55, v55
	v_fmac_f32_e32 v87, v23, v23
	v_fmac_f32_e32 v88, v19, v19
	v_fmac_f32_e32 v85, v52, v52
	v_fmac_f32_e32 v86, v56, v56
	v_fmac_f32_e32 v87, v24, v24
	v_fmac_f32_e32 v88, v20, v20
	v_fmac_f32_e32 v85, v53, v53
	v_fmac_f32_e32 v86, v57, v57
	v_fmac_f32_e32 v87, v25, v25
	v_fmac_f32_e32 v88, v21, v21
	v_fmac_f32_e32 v85, v14, v14
	v_fmac_f32_e32 v86, v10, v10
	v_fmac_f32_e32 v87, v6, v6
	v_fmac_f32_e32 v88, v2, v2
	v_fmac_f32_e32 v85, v15, v15
	v_fmac_f32_e32 v86, v11, v11
	v_fmac_f32_e32 v87, v7, v7
	v_fmac_f32_e32 v88, v3, v3
	v_fmac_f32_e32 v85, v16, v16
	v_fmac_f32_e32 v86, v12, v12
	v_fmac_f32_e32 v87, v8, v8
	v_fmac_f32_e32 v88, v4, v4
	v_fmac_f32_e32 v85, v17, v17
	v_fmac_f32_e32 v86, v13, v13
	v_fmac_f32_e32 v87, v9, v9
	v_fmac_f32_e32 v88, v5, v5
	v_add_f32_e32 v85, v85, v86
	v_add_f32_e32 v87, v87, v88
	v_add_f32_e32 v38, v85, v87
	s_nop 1
	v_add_f32_dpp v38, v38, v38 row_shr:1 row_mask:0xf bank_mask:0xf bound_ctrl:1
	s_nop 1
	v_add_f32_dpp v38, v38, v38 row_shr:2 row_mask:0xf bank_mask:0xf bound_ctrl:1
	s_nop 1
	v_add_f32_dpp v38, v38, v38 row_shr:4 row_mask:0xf bank_mask:0xf bound_ctrl:1
	s_nop 1
	v_add_f32_dpp v38, v38, v38 row_shr:8 row_mask:0xf bank_mask:0xf bound_ctrl:1
	s_nop 1
	v_mov_b32_dpp v40, v38 row_bcast:15 row_mask:0xa bank_mask:0xf
	v_add_f32_e32 v38, v38, v40
	s_nop 1
	v_mov_b32_dpp v84, v38 row_bcast:31 row_mask:0xc bank_mask:0xf
	v_add_f32_e32 v38, v38, v84
	s_nop 0
	v_readlane_b32 s10, v38, 63
	s_nop 1
	v_fma_f32 v38, s10, v46, v45
	v_mul_f32_e32 v39, 0x4b800000, v38
	v_cmp_gt_f32_e32 vcc, s18, v38
	s_nop 1
	v_cndmask_b32_e32 v38, v38, v39, vcc
	v_rsq_f32_e32 v40, v38
	v_lshl_add_u64 v[38:39], v[36:37], 0, s[2:3]
	v_mul_f32_e32 v70, 0x45800000, v40
	v_cndmask_b32_e32 v40, v40, v70, vcc
	v_pk_mul_f32 v[50:51], v[50:51], v[40:41] op_sel_hi:[1,0]
	v_pk_mul_f32 v[52:53], v[52:53], v[40:41] op_sel_hi:[1,0]
	v_pk_mul_f32 v[54:55], v[54:55], v[40:41] op_sel_hi:[1,0]
	v_pk_mul_f32 v[56:57], v[56:57], v[40:41] op_sel_hi:[1,0]
	v_pk_mul_f32 v[22:23], v[22:23], v[40:41] op_sel_hi:[1,0]
	v_pk_mul_f32 v[24:25], v[24:25], v[40:41] op_sel_hi:[1,0]
	v_pk_mul_f32 v[18:19], v[18:19], v[40:41] op_sel_hi:[1,0]
	v_pk_mul_f32 v[20:21], v[20:21], v[40:41] op_sel_hi:[1,0]
	v_pk_mul_f32 v[14:15], v[14:15], v[40:41] op_sel_hi:[1,0]
	v_pk_mul_f32 v[16:17], v[16:17], v[40:41] op_sel_hi:[1,0]
	v_pk_mul_f32 v[10:11], v[10:11], v[40:41] op_sel_hi:[1,0]
	v_pk_mul_f32 v[12:13], v[12:13], v[40:41] op_sel_hi:[1,0]
	v_pk_mul_f32 v[6:7], v[6:7], v[40:41] op_sel_hi:[1,0]
	v_pk_mul_f32 v[8:9], v[8:9], v[40:41] op_sel_hi:[1,0]
	v_pk_mul_f32 v[2:3], v[2:3], v[40:41] op_sel_hi:[1,0]
	v_pk_mul_f32 v[4:5], v[4:5], v[40:41] op_sel_hi:[1,0]
	v_pk_mul_f32 v[50:51], v[90:91], v[50:51]
	v_pk_mul_f32 v[52:53], v[92:93], v[52:53]
	v_pk_mul_f32 v[54:55], v[94:95], v[54:55]
	v_pk_mul_f32 v[56:57], v[96:97], v[56:57]
	v_pk_mul_f32 v[22:23], v[98:99], v[22:23]
	v_pk_mul_f32 v[24:25], v[100:101], v[24:25]
	v_pk_mul_f32 v[18:19], v[102:103], v[18:19]
	v_pk_mul_f32 v[20:21], v[104:105], v[20:21]
	v_pk_mul_f32 v[14:15], v[106:107], v[14:15]
	v_pk_mul_f32 v[16:17], v[108:109], v[16:17]
	v_pk_mul_f32 v[10:11], v[110:111], v[10:11]
	v_pk_mul_f32 v[12:13], v[112:113], v[12:13]
	v_pk_mul_f32 v[6:7], v[114:115], v[6:7]
	v_pk_mul_f32 v[8:9], v[116:117], v[8:9]
	v_pk_mul_f32 v[2:3], v[118:119], v[2:3]
	v_pk_mul_f32 v[4:5], v[120:121], v[4:5]
	s_waitcnt vmcnt(0)
	v_pk_add_f32 v[122:123], v[122:123], 1.0 op_sel_hi:[1,0]
	v_pk_add_f32 v[124:125], v[124:125], 1.0 op_sel_hi:[1,0]
	v_pk_fma_f32 v[50:51], v[122:123], v[50:51], v[154:155]
	v_pk_fma_f32 v[52:53], v[124:125], v[52:53], v[156:157]
	v_cvt_pk_bf16_f32 v50, v50, v51
	v_cvt_pk_bf16_f32 v51, v52, v53
	global_store_dwordx2 v[38:39], v[50:51], off
	v_pk_add_f32 v[126:127], v[126:127], 1.0 op_sel_hi:[1,0]
	v_pk_add_f32 v[128:129], v[128:129], 1.0 op_sel_hi:[1,0]
	v_pk_fma_f32 v[54:55], v[126:127], v[54:55], v[158:159]
	v_pk_fma_f32 v[56:57], v[128:129], v[56:57], v[160:161]
	v_cvt_pk_bf16_f32 v54, v54, v55
	v_cvt_pk_bf16_f32 v55, v56, v57
	global_store_dwordx2 v[38:39], v[54:55], off offset:512
	v_pk_add_f32 v[130:131], v[130:131], 1.0 op_sel_hi:[1,0]
	v_pk_add_f32 v[132:133], v[132:133], 1.0 op_sel_hi:[1,0]
	v_pk_fma_f32 v[22:23], v[130:131], v[22:23], v[162:163]
	v_pk_fma_f32 v[24:25], v[132:133], v[24:25], v[164:165]
	v_cvt_pk_bf16_f32 v22, v22, v23
	v_cvt_pk_bf16_f32 v23, v24, v25
	global_store_dwordx2 v[38:39], v[22:23], off offset:1024
	v_pk_add_f32 v[134:135], v[134:135], 1.0 op_sel_hi:[1,0]
	v_pk_add_f32 v[136:137], v[136:137], 1.0 op_sel_hi:[1,0]
	v_pk_fma_f32 v[18:19], v[134:135], v[18:19], v[166:167]
	v_pk_fma_f32 v[20:21], v[136:137], v[20:21], v[168:169]
	v_cvt_pk_bf16_f32 v18, v18, v19
	v_cvt_pk_bf16_f32 v19, v20, v21
	global_store_dwordx2 v[38:39], v[18:19], off offset:1536
	v_pk_add_f32 v[138:139], v[138:139], 1.0 op_sel_hi:[1,0]
	v_pk_add_f32 v[140:141], v[140:141], 1.0 op_sel_hi:[1,0]
	v_pk_fma_f32 v[14:15], v[138:139], v[14:15], v[170:171]
	v_pk_fma_f32 v[16:17], v[140:141], v[16:17], v[172:173]
	v_cvt_pk_bf16_f32 v14, v14, v15
	v_cvt_pk_bf16_f32 v15, v16, v17
	global_store_dwordx2 v[38:39], v[14:15], off offset:2048
	v_pk_add_f32 v[142:143], v[142:143], 1.0 op_sel_hi:[1,0]
	v_pk_add_f32 v[144:145], v[144:145], 1.0 op_sel_hi:[1,0]
	v_pk_fma_f32 v[10:11], v[142:143], v[10:11], v[174:175]
	v_pk_fma_f32 v[12:13], v[144:145], v[12:13], v[176:177]
	v_cvt_pk_bf16_f32 v10, v10, v11
	v_cvt_pk_bf16_f32 v11, v12, v13
	global_store_dwordx2 v[38:39], v[10:11], off offset:2560
	v_pk_add_f32 v[146:147], v[146:147], 1.0 op_sel_hi:[1,0]
	v_pk_add_f32 v[148:149], v[148:149], 1.0 op_sel_hi:[1,0]
	v_pk_fma_f32 v[6:7], v[146:147], v[6:7], v[178:179]
	v_pk_fma_f32 v[8:9], v[148:149], v[8:9], v[180:181]
	v_cvt_pk_bf16_f32 v6, v6, v7
	v_cvt_pk_bf16_f32 v7, v8, v9
	global_store_dwordx2 v[38:39], v[6:7], off offset:3072
	v_pk_add_f32 v[150:151], v[150:151], 1.0 op_sel_hi:[1,0]
	v_pk_add_f32 v[152:153], v[152:153], 1.0 op_sel_hi:[1,0]
	v_pk_fma_f32 v[2:3], v[150:151], v[2:3], v[182:183]
	v_pk_fma_f32 v[4:5], v[152:153], v[4:5], v[184:185]
	v_cvt_pk_bf16_f32 v2, v2, v3
	v_cvt_pk_bf16_f32 v3, v4, v5
	global_store_dwordx2 v[38:39], v[2:3], off offset:3584
	s_cbranch_scc0 .LBB0_93

; __device__ __forceinline__ unsigned pk2(float lo, float hi) { return f2bf(lo) | (f2bf(hi) << 16); }
; __device__ __forceinline__ void phase6(const Args& a, LAS unsigned char* lds, int tid, int lane, int wave, int vcu, int G) {
;     ...
;                 const int lr = wave * 4 + rr, t = blk * 64 + it * 32 + lr; const float* mr = mod + (size_t)(t >> 11) * 12288;
;                 const bf16* yr = Y1 + (size_t)t * 2048; const float* xr = a.in[0] + (size_t)t * 2048;
;     ...
;                 for (int j = 0; j < 8; ++j) { const int c = 4 * (lane + 64 * j); const f32x4 x = xv[j], gp = *(const f32x4*)(gpost + c), gt = *(const f32x4*)(mr + 4096 + c);
;                     const f32x4 x1 = x + gt * (y[j] * rstd1 * gp); y[j] = x1;
;                     v2u xb; xb.x = pk2(x1[0], x1[1]); xb.y = pk2(x1[2], x1[3]); __builtin_nontemporal_store(xb, (v2u*)(X1 + (size_t)t * 2048 + c));
;                     s2 += x1[0] * x1[0] + x1[1] * x1[1] + x1[2] * x1[2] + x1[3] * x1[3]; }
;                 const float rstd2 = rsqrtf(wave_sum(s2) * (1.f / 2048.f) + EPS);
; #pragma unroll
;                 for (int j = 0; j < 8; ++j) { const int c = 4 * (lane + 64 * j); const f32x4 g2 = *(const f32x4*)(gpre2 + c), sh = *(const f32x4*)(mr + 6144 + c), sc = *(const f32x4*)(mr + 8192 + c);
;                     const f32x4 hh = y[j] * rstd2 * g2 * (sc + 1.f) + sh;
.LBB0_1084:
	s_ashr_i32 s18, s51, 5
	s_mul_hi_i32 s19, s18, 0xc000
	s_mul_i32 s18, s18, 0xc000
	s_add_u32 s18, s33, s18
	s_addc_u32 s19, s38, s19
	s_add_u32 s20, s18, 0x4000
	s_addc_u32 s21, s19, 0
	s_add_u32 s18, s18, 0x8000
	s_addc_u32 s19, s19, 0
	v_lshlrev_b32_e32 v2, 4, v0
	v_and_b32_e32 v16, 0xffffffc0, v0
	v_lshlrev_b32_e32 v16, 4, v16
	v_lshl_add_u64 v[4:5], v[24:25], 0, v[16:17]
	v_lshl_add_u64 v[6:7], v[22:23], 0, v[16:17]
	global_load_dwordx4 v[100:103], v[4:5], off
	global_load_dwordx4 v[104:107], v2, s[20:21]
	global_load_dwordx4 v[108:111], v[6:7], off
	global_load_dwordx4 v[112:115], v2, s[18:19]
	s_waitcnt vmcnt(0)
	v_pk_mul_f32 v[100:101], v[100:101], v[104:105]
	v_pk_mul_f32 v[102:103], v[102:103], v[106:107]
	v_pk_add_f32 v[112:113], v[112:113], 1.0 op_sel_hi:[1,0]
	v_pk_add_f32 v[114:115], v[114:115], 1.0 op_sel_hi:[1,0]
	v_pk_mul_f32 v[108:109], v[108:109], v[112:113]
	v_pk_mul_f32 v[110:111], v[110:111], v[114:115]
	v_add_u32_e32 v3, 0x24000, v2
	ds_write_b128 v3, v[100:103]
	ds_write_b128 v3, v[108:111] offset:8192
	s_waitcnt lgkmcnt(0)
	s_barrier
	s_lshl_b32 s54, s51, 6
	s_mov_b64 s[16:17], -1
	s_mov_b32 s26, s35
	s_branch .LBB0_1086

; __device__ __forceinline__ void phase6(const Args& a, LAS unsigned char* lds, int tid, int lane, int wave, int vcu, int G) {
;     ...
;                 const int lr = wave * 4 + rr, t = blk * 64 + it * 32 + lr; const float* mr = mod + (size_t)(t >> 11) * 12288;
;                 const bf16* yr = Y1 + (size_t)t * 2048; const float* xr = a.in[0] + (size_t)t * 2048;
;                 f32x4 y[8], xv[8]; v2u ybv[8]; float ss = 0.f;
; #pragma unroll
;                 for (int j = 0; j < 8; ++j) { ybv[j] = __builtin_nontemporal_load((const v2u*)(yr + 4 * (lane + 64 * j))); xv[j] = __builtin_nontemporal_load((const f32x4*)(xr + 4 * (lane + 64 * j))); }
; #pragma unroll
;                 for (int j = 0; j < 8; ++j) { const v2u yb = ybv[j]; y[j] = (f32x4){bflo(yb.x), bfhi(yb.x), bflo(yb.y), bfhi(yb.y)}; ss += y[j][0] * y[j][0] + y[j][1] * y[j][1] + y[j][2] * y[j][2] + y[j][3] * y[j][3]; }
;                 const float rstd1 = rsqrtf(wave_sum(ss) * (1.f / 2048.f) + EPS);
.LBB0_1087:
	s_ashr_i32 s18, s16, 11
	s_ashr_i32 s17, s16, 31
	s_mul_hi_i32 s24, s18, 0xc000
	s_mul_i32 s25, s18, 0xc000
	s_lshl_b64 s[18:19], s[16:17], 11
	s_lshl_b64 s[20:21], s[16:17], 13
	s_add_u32 s20, s68, s20
	v_lshl_add_u64 v[100:101], v[96:97], 0, s[18:19]
	s_addc_u32 s21, s69, s21
	s_lshl_b64 s[18:19], s[16:17], 12
	v_lshl_add_u64 v[118:119], v[92:93], 0, s[18:19]
	v_lshl_add_u64 v[102:103], v[94:95], 0, s[18:19]
	global_load_dwordx2 v[156:157], v[118:119], off nt
	global_load_dwordx2 v[158:159], v[118:119], off offset:512 nt
	global_load_dwordx2 v[160:161], v[118:119], off offset:1024 nt
	global_load_dwordx2 v[162:163], v[118:119], off offset:1536 nt
	global_load_dwordx2 v[164:165], v[118:119], off offset:2048 nt
	global_load_dwordx2 v[166:167], v[118:119], off offset:2560 nt
	global_load_dwordx2 v[168:169], v[118:119], off offset:3072 nt
	global_load_dwordx2 v[170:171], v[118:119], off offset:3584 nt
	global_load_dwordx4 v[208:211], v128, s[20:21] nt
	global_load_dwordx4 v[212:215], v128, s[20:21] offset:1024 nt
	global_load_dwordx4 v[216:219], v128, s[20:21] offset:2048 nt
	global_load_dwordx4 v[220:223], v128, s[20:21] offset:3072 nt
	global_load_dwordx4 v[224:227], v129, s[20:21] nt
	global_load_dwordx4 v[228:231], v130, s[20:21] nt
	global_load_dwordx4 v[232:235], v131, s[20:21] nt
	global_load_dwordx4 v[236:239], v132, s[20:21] nt
	s_add_u32 s18, s33, s25
	s_addc_u32 s19, s38, s24
	s_add_u32 s18, s18, 0x6000
	s_addc_u32 s19, s19, 0
	global_load_dwordx4 v[172:175], v128, s[18:19]
	global_load_dwordx4 v[176:179], v128, s[18:19] offset:1024
	global_load_dwordx4 v[180:183], v128, s[18:19] offset:2048
	global_load_dwordx4 v[184:187], v128, s[18:19] offset:3072
	global_load_dwordx4 v[188:191], v129, s[18:19]
	global_load_dwordx4 v[192:195], v130, s[18:19]
	global_load_dwordx4 v[196:199], v131, s[18:19]
	global_load_dwordx4 v[200:203], v132, s[18:19]
	s_add_i32 s16, s16, 1
	v_add_u32_e32 v206, 0x24000, v128
	v_add_u32_e32 v207, s27, v127
	v_mov_b32_e32 v204, 0
	v_mov_b32_e32 v205, 0
	ds_read_b128 v[2:5], v206
	ds_read_b128 v[6:9], v206 offset:1024
	ds_read_b128 v[10:13], v206 offset:2048
	ds_read_b128 v[104:107], v206 offset:3072
	ds_read_b128 v[108:111], v206 offset:4096
	ds_read_b128 v[112:115], v206 offset:5120
	ds_read_b128 v[144:147], v206 offset:6144
	ds_read_b128 v[148:151], v206 offset:7168
	s_waitcnt vmcnt(16)
	v_lshlrev_b32_e32 v152, 16, v156
	v_and_b32_e32 v153, 0xffff0000, v156
	v_lshlrev_b32_e32 v154, 16, v157
	v_and_b32_e32 v155, 0xffff0000, v157
	v_mul_f32_e32 v240, v152, v152
	v_mul_f32_e32 v241, v153, v153
	v_mul_f32_e32 v242, v154, v154
	v_mul_f32_e32 v243, v155, v155
	v_lshlrev_b32_e32 v152, 16, v158
	v_and_b32_e32 v153, 0xffff0000, v158
	v_lshlrev_b32_e32 v154, 16, v159
	v_and_b32_e32 v155, 0xffff0000, v159
	v_fmac_f32_e32 v240, v152, v152
	v_fmac_f32_e32 v241, v153, v153
	v_fmac_f32_e32 v242, v154, v154
	v_fmac_f32_e32 v243, v155, v155
	v_lshlrev_b32_e32 v152, 16, v160
	v_and_b32_e32 v153, 0xffff0000, v160
	v_lshlrev_b32_e32 v154, 16, v161
	v_and_b32_e32 v155, 0xffff0000, v161
	v_fmac_f32_e32 v240, v152, v152
	v_fmac_f32_e32 v241, v153, v153
	v_fmac_f32_e32 v242, v154, v154
	v_fmac_f32_e32 v243, v155, v155
	v_lshlrev_b32_e32 v152, 16, v162
	v_and_b32_e32 v153, 0xffff0000, v162
	v_lshlrev_b32_e32 v154, 16, v163
	v_and_b32_e32 v155, 0xffff0000, v163
	v_fmac_f32_e32 v240, v152, v152
	v_fmac_f32_e32 v241, v153, v153
	v_fmac_f32_e32 v242, v154, v154
	v_fmac_f32_e32 v243, v155, v155
	v_lshlrev_b32_e32 v152, 16, v164
	v_and_b32_e32 v153, 0xffff0000, v164
	v_lshlrev_b32_e32 v154, 16, v165
	v_and_b32_e32 v155, 0xffff0000, v165
	v_fmac_f32_e32 v240, v152, v152
	v_fmac_f32_e32 v241, v153, v153
	v_fmac_f32_e32 v242, v154, v154
	v_fmac_f32_e32 v243, v155, v155
	v_lshlrev_b32_e32 v152, 16, v166
	v_and_b32_e32 v153, 0xffff0000, v166
	v_lshlrev_b32_e32 v154, 16, v167
	v_and_b32_e32 v155, 0xffff0000, v167
	v_fmac_f32_e32 v240, v152, v152
	v_fmac_f32_e32 v241, v153, v153
	v_fmac_f32_e32 v242, v154, v154
	v_fmac_f32_e32 v243, v155, v155
	v_lshlrev_b32_e32 v152, 16, v168
	v_and_b32_e32 v153, 0xffff0000, v168
	v_lshlrev_b32_e32 v154, 16, v169
	v_and_b32_e32 v155, 0xffff0000, v169
	v_fmac_f32_e32 v240, v152, v152
	v_fmac_f32_e32 v241, v153, v153
	v_fmac_f32_e32 v242, v154, v154
	v_fmac_f32_e32 v243, v155, v155
	v_lshlrev_b32_e32 v152, 16, v170
	v_and_b32_e32 v153, 0xffff0000, v170
	v_lshlrev_b32_e32 v154, 16, v171
	v_and_b32_e32 v155, 0xffff0000, v171
	v_fmac_f32_e32 v240, v152, v152
	v_fmac_f32_e32 v241, v153, v153
	v_fmac_f32_e32 v242, v154, v154
	v_fmac_f32_e32 v243, v155, v155
	v_add_f32_e32 v240, v240, v241
	v_add_f32_e32 v242, v242, v243
	v_add_f32_e32 v240, v240, v242
	s_nop 1
	v_add_f32_dpp v240, v240, v240 row_shr:1 row_mask:0xf bank_mask:0xf bound_ctrl:1
	s_nop 1
	v_add_f32_dpp v240, v240, v240 row_shr:2 row_mask:0xf bank_mask:0xf bound_ctrl:1
	s_nop 1
	v_add_f32_dpp v240, v240, v240 row_shr:4 row_mask:0xf bank_mask:0xf bound_ctrl:1
	s_nop 1
	v_add_f32_dpp v240, v240, v240 row_shr:8 row_mask:0xf bank_mask:0xf bound_ctrl:1
	s_nop 1
	v_mov_b32_dpp v204, v240 row_bcast:15 row_mask:0xa bank_mask:0xf
	v_add_f32_e32 v240, v240, v204
	s_nop 1
	v_mov_b32_dpp v205, v240 row_bcast:31 row_mask:0xc bank_mask:0xf
	v_add_f32_e32 v240, v240, v205
	s_nop 0
	v_readlane_b32 s17, v240, 63
	s_nop 1
	v_fma_f32 v16, s17, v140, v133
	v_mul_f32_e32 v244, 0x4b800000, v16
	v_cmp_gt_f32_e32 vcc, s48, v16
	s_nop 1
	v_cndmask_b32_e32 v16, v16, v244, vcc
	v_rsq_f32_e32 v16, v16
	s_nop 0
	v_mul_f32_e32 v244, 0x45800000, v16
	v_cndmask_b32_e32 v16, v16, v244, vcc
	s_waitcnt vmcnt(8) lgkmcnt(0)
; __device__ __forceinline__ unsigned pk2(float lo, float hi) { return f2bf(lo) | (f2bf(hi) << 16); }
; __device__ __forceinline__ void phase6(const Args& a, LAS unsigned char* lds, int tid, int lane, int wave, int vcu, int G) {
;     ...
;                 float s2 = 0.f;
; #pragma unroll
;                 for (int j = 0; j < 8; ++j) { const int c = 4 * (lane + 64 * j); const f32x4 x = xv[j], gp = *(const f32x4*)(gpost + c), gt = *(const f32x4*)(mr + 4096 + c);
;                     const f32x4 x1 = x + gt * (y[j] * rstd1 * gp); y[j] = x1;
;                     v2u xb; xb.x = pk2(x1[0], x1[1]); xb.y = pk2(x1[2], x1[3]); __builtin_nontemporal_store(xb, (v2u*)(X1 + (size_t)t * 2048 + c));
;                     s2 += x1[0] * x1[0] + x1[1] * x1[1] + x1[2] * x1[2] + x1[3] * x1[3]; }
;                 const float rstd2 = rsqrtf(wave_sum(s2) * (1.f / 2048.f) + EPS);
	v_lshlrev_b32_e32 v152, 16, v156
	v_and_b32_e32 v153, 0xffff0000, v156
	v_lshlrev_b32_e32 v154, 16, v157
	v_and_b32_e32 v155, 0xffff0000, v157
	v_pk_mul_f32 v[152:153], v[152:153], v[16:17] op_sel_hi:[1,0]
	v_pk_mul_f32 v[154:155], v[154:155], v[16:17] op_sel_hi:[1,0]
	v_pk_fma_f32 v[208:209], v[2:3], v[152:153], v[208:209]
	v_pk_fma_f32 v[210:211], v[4:5], v[154:155], v[210:211]
	v_mul_f32_e32 v240, v208, v208
	v_mul_f32_e32 v241, v209, v209
	v_mul_f32_e32 v242, v210, v210
	v_mul_f32_e32 v243, v211, v211
	v_cvt_pk_bf16_f32 v120, v208, v209
	v_cvt_pk_bf16_f32 v121, v210, v211
	global_store_dwordx2 v[102:103], v[120:121], off nt
	v_lshlrev_b32_e32 v152, 16, v158
	v_and_b32_e32 v153, 0xffff0000, v158
	v_lshlrev_b32_e32 v154, 16, v159
	v_and_b32_e32 v155, 0xffff0000, v159
	v_pk_mul_f32 v[152:153], v[152:153], v[16:17] op_sel_hi:[1,0]
	v_pk_mul_f32 v[154:155], v[154:155], v[16:17] op_sel_hi:[1,0]
	v_pk_fma_f32 v[212:213], v[6:7], v[152:153], v[212:213]
	v_pk_fma_f32 v[214:215], v[8:9], v[154:155], v[214:215]
	v_fmac_f32_e32 v240, v212, v212
	v_fmac_f32_e32 v241, v213, v213
	v_fmac_f32_e32 v242, v214, v214
	v_fmac_f32_e32 v243, v215, v215
	v_cvt_pk_bf16_f32 v116, v212, v213
	v_cvt_pk_bf16_f32 v117, v214, v215
	global_store_dwordx2 v[102:103], v[116:117], off offset:512 nt
	v_lshlrev_b32_e32 v152, 16, v160
	v_and_b32_e32 v153, 0xffff0000, v160
	v_lshlrev_b32_e32 v154, 16, v161
	v_and_b32_e32 v155, 0xffff0000, v161
	v_pk_mul_f32 v[152:153], v[152:153], v[16:17] op_sel_hi:[1,0]
	v_pk_mul_f32 v[154:155], v[154:155], v[16:17] op_sel_hi:[1,0]
	v_pk_fma_f32 v[216:217], v[10:11], v[152:153], v[216:217]
	v_pk_fma_f32 v[218:219], v[12:13], v[154:155], v[218:219]
	v_fmac_f32_e32 v240, v216, v216
	v_fmac_f32_e32 v241, v217, v217
	v_fmac_f32_e32 v242, v218, v218
	v_fmac_f32_e32 v243, v219, v219
	v_cvt_pk_bf16_f32 v120, v216, v217
	v_cvt_pk_bf16_f32 v121, v218, v219
	global_store_dwordx2 v[102:103], v[120:121], off offset:1024 nt
	v_lshlrev_b32_e32 v152, 16, v162
	v_and_b32_e32 v153, 0xffff0000, v162
	v_lshlrev_b32_e32 v154, 16, v163
	v_and_b32_e32 v155, 0xffff0000, v163
	v_pk_mul_f32 v[152:153], v[152:153], v[16:17] op_sel_hi:[1,0]
	v_pk_mul_f32 v[154:155], v[154:155], v[16:17] op_sel_hi:[1,0]
	v_pk_fma_f32 v[220:221], v[104:105], v[152:153], v[220:221]
	v_pk_fma_f32 v[222:223], v[106:107], v[154:155], v[222:223]
	v_fmac_f32_e32 v240, v220, v220
	v_fmac_f32_e32 v241, v221, v221
	v_fmac_f32_e32 v242, v222, v222
	v_fmac_f32_e32 v243, v223, v223
	v_cvt_pk_bf16_f32 v116, v220, v221
	v_cvt_pk_bf16_f32 v117, v222, v223
	global_store_dwordx2 v[102:103], v[116:117], off offset:1536 nt
	v_lshlrev_b32_e32 v152, 16, v164
	v_and_b32_e32 v153, 0xffff0000, v164
	v_lshlrev_b32_e32 v154, 16, v165
	v_and_b32_e32 v155, 0xffff0000, v165
	v_pk_mul_f32 v[152:153], v[152:153], v[16:17] op_sel_hi:[1,0]
	v_pk_mul_f32 v[154:155], v[154:155], v[16:17] op_sel_hi:[1,0]
	v_pk_fma_f32 v[224:225], v[108:109], v[152:153], v[224:225]
	v_pk_fma_f32 v[226:227], v[110:111], v[154:155], v[226:227]
	v_fmac_f32_e32 v240, v224, v224
	v_fmac_f32_e32 v241, v225, v225
	v_fmac_f32_e32 v242, v226, v226
	v_fmac_f32_e32 v243, v227, v227
	v_cvt_pk_bf16_f32 v120, v224, v225
	v_cvt_pk_bf16_f32 v121, v226, v227
	global_store_dwordx2 v[102:103], v[120:121], off offset:2048 nt
	v_lshlrev_b32_e32 v152, 16, v166
	v_and_b32_e32 v153, 0xffff0000, v166
	v_lshlrev_b32_e32 v154, 16, v167
	v_and_b32_e32 v155, 0xffff0000, v167
	v_pk_mul_f32 v[152:153], v[152:153], v[16:17] op_sel_hi:[1,0]
	v_pk_mul_f32 v[154:155], v[154:155], v[16:17] op_sel_hi:[1,0]
	v_pk_fma_f32 v[228:229], v[112:113], v[152:153], v[228:229]
	v_pk_fma_f32 v[230:231], v[114:115], v[154:155], v[230:231]
	v_fmac_f32_e32 v240, v228, v228
	v_fmac_f32_e32 v241, v229, v229
	v_fmac_f32_e32 v242, v230, v230
	v_fmac_f32_e32 v243, v231, v231
	v_cvt_pk_bf16_f32 v116, v228, v229
	v_cvt_pk_bf16_f32 v117, v230, v231
	global_store_dwordx2 v[102:103], v[116:117], off offset:2560 nt
	v_lshlrev_b32_e32 v152, 16, v168
	v_and_b32_e32 v153, 0xffff0000, v168
	v_lshlrev_b32_e32 v154, 16, v169
	v_and_b32_e32 v155, 0xffff0000, v169
	v_pk_mul_f32 v[152:153], v[152:153], v[16:17] op_sel_hi:[1,0]
	v_pk_mul_f32 v[154:155], v[154:155], v[16:17] op_sel_hi:[1,0]
	v_pk_fma_f32 v[232:233], v[144:145], v[152:153], v[232:233]
	v_pk_fma_f32 v[234:235], v[146:147], v[154:155], v[234:235]
	v_fmac_f32_e32 v240, v232, v232
	v_fmac_f32_e32 v241, v233, v233
	v_fmac_f32_e32 v242, v234, v234
	v_fmac_f32_e32 v243, v235, v235
	v_cvt_pk_bf16_f32 v120, v232, v233
	v_cvt_pk_bf16_f32 v121, v234, v235
	global_store_dwordx2 v[102:103], v[120:121], off offset:3072 nt
	v_lshlrev_b32_e32 v152, 16, v170
	v_and_b32_e32 v153, 0xffff0000, v170
	v_lshlrev_b32_e32 v154, 16, v171
	v_and_b32_e32 v155, 0xffff0000, v171
	v_pk_mul_f32 v[152:153], v[152:153], v[16:17] op_sel_hi:[1,0]
	v_pk_mul_f32 v[154:155], v[154:155], v[16:17] op_sel_hi:[1,0]
	v_pk_fma_f32 v[236:237], v[148:149], v[152:153], v[236:237]
	v_pk_fma_f32 v[238:239], v[150:151], v[154:155], v[238:239]
	v_fmac_f32_e32 v240, v236, v236
	v_fmac_f32_e32 v241, v237, v237
	v_fmac_f32_e32 v242, v238, v238
	v_fmac_f32_e32 v243, v239, v239
	v_cvt_pk_bf16_f32 v116, v236, v237
	v_cvt_pk_bf16_f32 v117, v238, v239
	global_store_dwordx2 v[102:103], v[116:117], off offset:3584 nt
	ds_read_b128 v[2:5], v206 offset:8192
	ds_read_b128 v[6:9], v206 offset:9216
	ds_read_b128 v[10:13], v206 offset:10240
	ds_read_b128 v[104:107], v206 offset:11264
	ds_read_b128 v[108:111], v206 offset:12288
	ds_read_b128 v[112:115], v206 offset:13312
	ds_read_b128 v[144:147], v206 offset:14336
	ds_read_b128 v[148:151], v206 offset:15360
	v_add_f32_e32 v240, v240, v241
	v_add_f32_e32 v242, v242, v243
	v_add_f32_e32 v240, v240, v242
	s_nop 1
	v_add_f32_dpp v240, v240, v240 row_shr:1 row_mask:0xf bank_mask:0xf bound_ctrl:1
	s_nop 1
	v_add_f32_dpp v240, v240, v240 row_shr:2 row_mask:0xf bank_mask:0xf bound_ctrl:1
	s_nop 1
	v_add_f32_dpp v240, v240, v240 row_shr:4 row_mask:0xf bank_mask:0xf bound_ctrl:1
	s_nop 1
	v_add_f32_dpp v240, v240, v240 row_shr:8 row_mask:0xf bank_mask:0xf bound_ctrl:1
	s_nop 1
	v_mov_b32_dpp v204, v240 row_bcast:15 row_mask:0xa bank_mask:0xf
	v_add_f32_e32 v240, v240, v204
	s_nop 1
	v_mov_b32_dpp v205, v240 row_bcast:31 row_mask:0xc bank_mask:0xf
	v_add_f32_e32 v240, v240, v205
	s_nop 0
	v_readlane_b32 s17, v240, 63
	s_nop 1
	v_fma_f32 v16, s17, v140, v133
	v_mul_f32_e32 v244, 0x4b800000, v16
	v_cmp_gt_f32_e32 vcc, s48, v16
	s_nop 1
	v_cndmask_b32_e32 v16, v16, v244, vcc
	v_rsq_f32_e32 v16, v16
	s_nop 0
	v_mul_f32_e32 v244, 0x45800000, v16
	v_cndmask_b32_e32 v16, v16, v244, vcc
	s_waitcnt vmcnt(8) lgkmcnt(0)
; #define LAS __attribute__((address_space(3)))
; __device__ __forceinline__ unsigned pk2(float lo, float hi) { return f2bf(lo) | (f2bf(hi) << 16); }
; __device__ __forceinline__ void phase6(const Args& a, LAS unsigned char* lds, int tid, int lane, int wave, int vcu, int G) {
;     ...
; #pragma unroll
;                 for (int j = 0; j < 8; ++j) { const int c = 4 * (lane + 64 * j); const f32x4 g2 = *(const f32x4*)(gpre2 + c), sh = *(const f32x4*)(mr + 6144 + c), sc = *(const f32x4*)(mr + 8192 + c);
;                     const f32x4 hh = y[j] * rstd2 * g2 * (sc + 1.f) + sh;
;                     v2u qh; qh.x = pk2(hh[0], hh[1]); qh.y = pk2(hh[2], hh[3]);
;                     *(LAS v2u*)(lds + RT_HI + lr * RT_ROWB + c * 2) = qh;
;                     *(unsigned*)(H2 + (size_t)t * 2048 + c) = pk4_fp8(hh[0] * SC_H, hh[1] * SC_H, hh[2] * SC_H, hh[3] * SC_H); }
;             }
	v_pk_mul_f32 v[208:209], v[208:209], v[16:17] op_sel_hi:[1,0]
	v_pk_mul_f32 v[210:211], v[210:211], v[16:17] op_sel_hi:[1,0]
	v_pk_fma_f32 v[208:209], v[208:209], v[2:3], v[172:173]
	v_pk_fma_f32 v[210:211], v[210:211], v[4:5], v[174:175]
	v_cvt_pk_bf16_f32 v120, v208, v209
	v_cvt_pk_bf16_f32 v121, v210, v211
	ds_write_b64 v207, v[120:121]
	v_mul_f32_e32 v152, 0x41800000, v208
	v_mul_f32_e32 v153, 0x41800000, v209
	v_mul_f32_e32 v154, 0x41800000, v210
	v_mul_f32_e32 v155, 0x41800000, v211
	v_med3_f32 v152, v152, s50, v142
	v_med3_f32 v153, v153, s50, v142
	v_med3_f32 v154, v154, s50, v142
	v_med3_f32 v155, v155, s50, v142
	v_cvt_pk_fp8_f32 v245, v152, v153
	s_nop 0
	v_cvt_pk_fp8_f32 v245, v154, v155 op_sel:[0,0,1]
	global_store_dword v[100:101], v245, off
	v_pk_mul_f32 v[212:213], v[212:213], v[16:17] op_sel_hi:[1,0]
	v_pk_mul_f32 v[214:215], v[214:215], v[16:17] op_sel_hi:[1,0]
	v_pk_fma_f32 v[212:213], v[212:213], v[6:7], v[176:177]
	v_pk_fma_f32 v[214:215], v[214:215], v[8:9], v[178:179]
	v_cvt_pk_bf16_f32 v116, v212, v213
	v_cvt_pk_bf16_f32 v117, v214, v215
	ds_write_b64 v207, v[116:117] offset:512
	v_mul_f32_e32 v152, 0x41800000, v212
	v_mul_f32_e32 v153, 0x41800000, v213
	v_mul_f32_e32 v154, 0x41800000, v214
	v_mul_f32_e32 v155, 0x41800000, v215
	v_med3_f32 v152, v152, s50, v142
	v_med3_f32 v153, v153, s50, v142
	v_med3_f32 v154, v154, s50, v142
	v_med3_f32 v155, v155, s50, v142
	v_cvt_pk_fp8_f32 v244, v152, v153
	s_nop 0
	v_cvt_pk_fp8_f32 v244, v154, v155 op_sel:[0,0,1]
	global_store_dword v[100:101], v244, off offset:256
	v_pk_mul_f32 v[216:217], v[216:217], v[16:17] op_sel_hi:[1,0]
	v_pk_mul_f32 v[218:219], v[218:219], v[16:17] op_sel_hi:[1,0]
	v_pk_fma_f32 v[216:217], v[216:217], v[10:11], v[180:181]
	v_pk_fma_f32 v[218:219], v[218:219], v[12:13], v[182:183]
	v_cvt_pk_bf16_f32 v120, v216, v217
	v_cvt_pk_bf16_f32 v121, v218, v219
	ds_write_b64 v207, v[120:121] offset:1024
	v_mul_f32_e32 v152, 0x41800000, v216
	v_mul_f32_e32 v153, 0x41800000, v217
	v_mul_f32_e32 v154, 0x41800000, v218
	v_mul_f32_e32 v155, 0x41800000, v219
	v_med3_f32 v152, v152, s50, v142
	v_med3_f32 v153, v153, s50, v142
	v_med3_f32 v154, v154, s50, v142
	v_med3_f32 v155, v155, s50, v142
	v_cvt_pk_fp8_f32 v245, v152, v153
	s_nop 0
	v_cvt_pk_fp8_f32 v245, v154, v155 op_sel:[0,0,1]
	global_store_dword v[100:101], v245, off offset:512
	v_pk_mul_f32 v[220:221], v[220:221], v[16:17] op_sel_hi:[1,0]
	v_pk_mul_f32 v[222:223], v[222:223], v[16:17] op_sel_hi:[1,0]
	v_pk_fma_f32 v[220:221], v[220:221], v[104:105], v[184:185]
	v_pk_fma_f32 v[222:223], v[222:223], v[106:107], v[186:187]
	v_cvt_pk_bf16_f32 v116, v220, v221
	v_cvt_pk_bf16_f32 v117, v222, v223
	ds_write_b64 v207, v[116:117] offset:1536
	v_mul_f32_e32 v152, 0x41800000, v220
	v_mul_f32_e32 v153, 0x41800000, v221
	v_mul_f32_e32 v154, 0x41800000, v222
	v_mul_f32_e32 v155, 0x41800000, v223
	v_med3_f32 v152, v152, s50, v142
	v_med3_f32 v153, v153, s50, v142
	v_med3_f32 v154, v154, s50, v142
	v_med3_f32 v155, v155, s50, v142
	v_cvt_pk_fp8_f32 v244, v152, v153
	s_nop 0
	v_cvt_pk_fp8_f32 v244, v154, v155 op_sel:[0,0,1]
	global_store_dword v[100:101], v244, off offset:768
	v_pk_mul_f32 v[224:225], v[224:225], v[16:17] op_sel_hi:[1,0]
	v_pk_mul_f32 v[226:227], v[226:227], v[16:17] op_sel_hi:[1,0]
	v_pk_fma_f32 v[224:225], v[224:225], v[108:109], v[188:189]
	v_pk_fma_f32 v[226:227], v[226:227], v[110:111], v[190:191]
	v_cvt_pk_bf16_f32 v120, v224, v225
	v_cvt_pk_bf16_f32 v121, v226, v227
	ds_write_b64 v207, v[120:121] offset:2048
	v_mul_f32_e32 v152, 0x41800000, v224
	v_mul_f32_e32 v153, 0x41800000, v225
	v_mul_f32_e32 v154, 0x41800000, v226
	v_mul_f32_e32 v155, 0x41800000, v227
	v_med3_f32 v152, v152, s50, v142
	v_med3_f32 v153, v153, s50, v142
	v_med3_f32 v154, v154, s50, v142
	v_med3_f32 v155, v155, s50, v142
	v_cvt_pk_fp8_f32 v245, v152, v153
	s_nop 0
	v_cvt_pk_fp8_f32 v245, v154, v155 op_sel:[0,0,1]
	global_store_dword v[100:101], v245, off offset:1024
	v_pk_mul_f32 v[228:229], v[228:229], v[16:17] op_sel_hi:[1,0]
	v_pk_mul_f32 v[230:231], v[230:231], v[16:17] op_sel_hi:[1,0]
	v_pk_fma_f32 v[228:229], v[228:229], v[112:113], v[192:193]
	v_pk_fma_f32 v[230:231], v[230:231], v[114:115], v[194:195]
	v_cvt_pk_bf16_f32 v116, v228, v229
	v_cvt_pk_bf16_f32 v117, v230, v231
	ds_write_b64 v207, v[116:117] offset:2560
	v_mul_f32_e32 v152, 0x41800000, v228
	v_mul_f32_e32 v153, 0x41800000, v229
	v_mul_f32_e32 v154, 0x41800000, v230
	v_mul_f32_e32 v155, 0x41800000, v231
	v_med3_f32 v152, v152, s50, v142
	v_med3_f32 v153, v153, s50, v142
	v_med3_f32 v154, v154, s50, v142
	v_med3_f32 v155, v155, s50, v142
	v_cvt_pk_fp8_f32 v244, v152, v153
	s_nop 0
	v_cvt_pk_fp8_f32 v244, v154, v155 op_sel:[0,0,1]
	global_store_dword v[100:101], v244, off offset:1280
	v_pk_mul_f32 v[232:233], v[232:233], v[16:17] op_sel_hi:[1,0]
	v_pk_mul_f32 v[234:235], v[234:235], v[16:17] op_sel_hi:[1,0]
	v_pk_fma_f32 v[232:233], v[232:233], v[144:145], v[196:197]
	v_pk_fma_f32 v[234:235], v[234:235], v[146:147], v[198:199]
	v_cvt_pk_bf16_f32 v120, v232, v233
	v_cvt_pk_bf16_f32 v121, v234, v235
	ds_write_b64 v207, v[120:121] offset:3072
	v_mul_f32_e32 v152, 0x41800000, v232
	v_mul_f32_e32 v153, 0x41800000, v233
	v_mul_f32_e32 v154, 0x41800000, v234
	v_mul_f32_e32 v155, 0x41800000, v235
	v_med3_f32 v152, v152, s50, v142
	v_med3_f32 v153, v153, s50, v142
	v_med3_f32 v154, v154, s50, v142
	v_med3_f32 v155, v155, s50, v142
	v_cvt_pk_fp8_f32 v245, v152, v153
	s_nop 0
	v_cvt_pk_fp8_f32 v245, v154, v155 op_sel:[0,0,1]
	global_store_dword v[100:101], v245, off offset:1536
	v_pk_mul_f32 v[236:237], v[236:237], v[16:17] op_sel_hi:[1,0]
	v_pk_mul_f32 v[238:239], v[238:239], v[16:17] op_sel_hi:[1,0]
	v_pk_fma_f32 v[236:237], v[236:237], v[148:149], v[200:201]
	v_pk_fma_f32 v[238:239], v[238:239], v[150:151], v[202:203]
	v_cvt_pk_bf16_f32 v116, v236, v237
	v_cvt_pk_bf16_f32 v117, v238, v239
	ds_write_b64 v207, v[116:117] offset:3584
	v_mul_f32_e32 v152, 0x41800000, v236
	v_mul_f32_e32 v153, 0x41800000, v237
	v_mul_f32_e32 v154, 0x41800000, v238
	v_mul_f32_e32 v155, 0x41800000, v239
	v_med3_f32 v152, v152, s50, v142
	v_med3_f32 v153, v153, s50, v142
	v_med3_f32 v154, v154, s50, v142
	v_med3_f32 v155, v155, s50, v142
	v_cvt_pk_fp8_f32 v244, v152, v153
	s_nop 0
	v_cvt_pk_fp8_f32 v244, v154, v155 op_sel:[0,0,1]
	global_store_dword v[100:101], v244, off offset:1792
	s_addk_i32 s27, 0x1010
	s_cmpk_eq_i32 s27, 0x4040
	s_cbranch_scc0 .LBB0_1087
; #define LAS __attribute__((address_space(3)))
; __device__ __forceinline__ void phase6(const Args& a, LAS unsigned char* lds, int tid, int lane, int wave, int vcu, int G) {
;     ...
; #pragma unroll
;             for (int k8 = 4; k8 < 8; ++k8) { const int k0 = 256 * wave + 32 * k8 + 8 * l4;
; #pragma unroll
;                 for (int et = 0; et < 4; ++et) bh[k8][et] = *(const bf16x8*)(whi + (size_t)(16 * et + l15) * 2048 + k0); }
;             { f32x4 acc[2][4];
; #pragma unroll
;               for (int mt = 0; mt < 2; ++mt)
; #pragma unroll
;                   for (int et = 0; et < 4; ++et) acc[mt][et] = (f32x4){0.f, 0.f, 0.f, 0.f};
; #pragma unroll
;               for (int k8 = 0; k8 < 8; ++k8) { const int k0 = 256 * wave + 32 * k8 + 8 * l4;
; #pragma unroll
;                   for (int mt = 0; mt < 2; ++mt) { const bf16x8 ah = *(const LAS bf16x8*)(lds + RT_HI + (16 * mt + l15) * RT_ROWB + k0 * 2);
; #pragma unroll
;                       for (int et = 0; et < 4; ++et) acc[mt][et] = __builtin_amdgcn_mfma_f32_16x16x32_bf16(ah, bh[k8][et], acc[mt][et], 0, 0, 0); } }
	global_load_dwordx4 v[2:5], v[42:43], off
	global_load_dwordx4 v[6:9], v[44:45], off
	global_load_dwordx4 v[10:13], v[46:47], off
	global_load_dwordx4 v[100:103], v[48:49], off
	global_load_dwordx4 v[104:107], v[42:43], off offset:64
	global_load_dwordx4 v[108:111], v[50:51], off
	global_load_dwordx4 v[112:115], v[52:53], off
	global_load_dwordx4 v[116:119], v[54:55], off
	global_load_dwordx4 v[144:147], v[56:57], off
	global_load_dwordx4 v[148:151], v[58:59], off
	global_load_dwordx4 v[152:155], v[42:43], off offset:128
	global_load_dwordx4 v[156:159], v[42:43], off offset:192
	global_load_dwordx4 v[160:163], v[60:61], off
	global_load_dwordx4 v[164:167], v[62:63], off
	global_load_dwordx4 v[168:171], v[64:65], off
	global_load_dwordx4 v[172:175], v[66:67], off
	s_waitcnt lgkmcnt(0)
	s_barrier
	ds_read_b128 v[176:179], v137
	ds_read_b128 v[180:183], v137 offset:64
	ds_read_b128 v[196:199], v138
	ds_read_b128 v[200:203], v138 offset:64
	v_add_u32_e32 v16, 0x1000, v139
	s_lshl_b32 s16, s26, 3
	s_or_b32 s27, s26, s54
	s_add_i32 s26, s16, 0
	s_add_i32 s26, s26, 0x22200
	s_mov_b32 s28, 0
	s_waitcnt vmcnt(15) lgkmcnt(3)
	v_mfma_f32_16x16x32_bf16 v[184:187], v[176:179], v[2:5], 0
	s_waitcnt vmcnt(14)
	v_mfma_f32_16x16x32_bf16 v[188:191], v[176:179], v[6:9], 0
	s_waitcnt vmcnt(13)
	v_mfma_f32_16x16x32_bf16 v[192:195], v[176:179], v[10:13], 0
	s_waitcnt vmcnt(12)
	v_mfma_f32_16x16x32_bf16 v[176:179], v[176:179], v[100:103], 0
	s_waitcnt lgkmcnt(1)
	v_mfma_f32_16x16x32_bf16 v[2:5], v[196:199], v[2:5], 0
	v_mfma_f32_16x16x32_bf16 v[6:9], v[196:199], v[6:9], 0
	v_mfma_f32_16x16x32_bf16 v[10:13], v[196:199], v[10:13], 0
	v_mfma_f32_16x16x32_bf16 v[100:103], v[196:199], v[100:103], 0
	s_waitcnt vmcnt(11)
	v_mfma_f32_16x16x32_bf16 v[184:187], v[180:183], v[104:107], v[184:187]
	s_waitcnt vmcnt(10)
	v_mfma_f32_16x16x32_bf16 v[188:191], v[180:183], v[108:111], v[188:191]
	s_waitcnt vmcnt(9)
	v_mfma_f32_16x16x32_bf16 v[192:195], v[180:183], v[112:115], v[192:195]
	s_waitcnt vmcnt(8)
	v_mfma_f32_16x16x32_bf16 v[176:179], v[180:183], v[116:119], v[176:179]
	s_waitcnt lgkmcnt(0)
	v_mfma_f32_16x16x32_bf16 v[2:5], v[200:203], v[104:107], v[2:5]
	v_mfma_f32_16x16x32_bf16 v[6:9], v[200:203], v[108:111], v[6:9]
	ds_read_b128 v[104:107], v137 offset:128
	ds_read_b128 v[108:111], v137 offset:192
	v_mfma_f32_16x16x32_bf16 v[10:13], v[200:203], v[112:115], v[10:13]
	v_mfma_f32_16x16x32_bf16 v[100:103], v[200:203], v[116:119], v[100:103]
	s_waitcnt vmcnt(5) lgkmcnt(1)
	v_mfma_f32_16x16x32_bf16 v[112:115], v[104:107], v[152:155], v[184:187]
	v_mfma_f32_16x16x32_bf16 v[116:119], v[104:107], v[144:147], v[188:191]
	v_mfma_f32_16x16x32_bf16 v[180:183], v[104:107], v[148:151], v[192:195]
	s_waitcnt vmcnt(3)
	v_mfma_f32_16x16x32_bf16 v[104:107], v[104:107], v[160:163], v[176:179]
	s_nop 2
	ds_read_b128 v[176:179], v138 offset:128
	ds_read_b128 v[184:187], v138 offset:192
	s_waitcnt lgkmcnt(1)
	v_mfma_f32_16x16x32_bf16 v[6:9], v[176:179], v[144:147], v[6:9]
	v_mfma_f32_16x16x32_bf16 v[10:13], v[176:179], v[148:151], v[10:13]
	global_load_dwordx4 v[148:151], v[68:69], off
	v_mfma_f32_16x16x32_bf16 v[2:5], v[176:179], v[152:155], v[2:5]
	ds_read_b128 v[152:155], v137 offset:256
	v_mfma_f32_16x16x32_bf16 v[112:115], v[108:111], v[156:159], v[112:115]
	s_waitcnt vmcnt(3)
	v_mfma_f32_16x16x32_bf16 v[116:119], v[108:111], v[164:167], v[116:119]
	s_waitcnt vmcnt(2)
	v_mfma_f32_16x16x32_bf16 v[144:147], v[108:111], v[168:171], v[180:183]
	s_waitcnt vmcnt(1)
	v_mfma_f32_16x16x32_bf16 v[104:107], v[108:111], v[172:175], v[104:107]
	global_load_dwordx4 v[108:111], v[42:43], off offset:256
	s_waitcnt lgkmcnt(1)
	v_mfma_f32_16x16x32_bf16 v[6:9], v[184:187], v[164:167], v[6:9]
	global_load_dwordx4 v[164:167], v[70:71], off
	v_mfma_f32_16x16x32_bf16 v[10:13], v[184:187], v[168:171], v[10:13]
	global_load_dwordx4 v[168:171], v[72:73], off
	v_mfma_f32_16x16x32_bf16 v[2:5], v[184:187], v[156:159], v[2:5]
	global_load_dwordx4 v[156:159], v[42:43], off offset:320
	v_mfma_f32_16x16x32_bf16 v[100:103], v[176:179], v[160:163], v[100:103]
	ds_read_b128 v[160:163], v137 offset:320
	v_mfma_f32_16x16x32_bf16 v[100:103], v[184:187], v[172:175], v[100:103]
	global_load_dwordx4 v[172:175], v[74:75], off
	s_waitcnt vmcnt(4) lgkmcnt(1)
	v_mfma_f32_16x16x32_bf16 v[112:115], v[152:155], v[108:111], v[112:115]
	v_mfma_f32_16x16x32_bf16 v[116:119], v[152:155], v[148:151], v[116:119]
	s_waitcnt vmcnt(3)
	v_mfma_f32_16x16x32_bf16 v[144:147], v[152:155], v[164:167], v[144:147]
	s_waitcnt vmcnt(2)
	v_mfma_f32_16x16x32_bf16 v[104:107], v[152:155], v[168:171], v[104:107]
	ds_read_b128 v[152:155], v138 offset:256
	ds_read_b128 v[176:179], v138 offset:320
	s_waitcnt lgkmcnt(1)
	v_mfma_f32_16x16x32_bf16 v[2:5], v[152:155], v[108:111], v[2:5]
	s_waitcnt vmcnt(1)
	v_mfma_f32_16x16x32_bf16 v[108:111], v[160:163], v[156:159], v[112:115]
	s_nop 2
	global_load_dwordx4 v[112:115], v[76:77], off
	v_mfma_f32_16x16x32_bf16 v[6:9], v[152:155], v[148:151], v[6:9]
	global_load_dwordx4 v[148:151], v[78:79], off
	v_mfma_f32_16x16x32_bf16 v[10:13], v[152:155], v[164:167], v[10:13]
	global_load_dwordx4 v[164:167], v[82:83], off
	v_mfma_f32_16x16x32_bf16 v[100:103], v[152:155], v[168:171], v[100:103]
	global_load_dwordx4 v[152:155], v[42:43], off offset:384
	global_load_dwordx4 v[168:171], v[84:85], off
	s_waitcnt vmcnt(4)
	v_mfma_f32_16x16x32_bf16 v[144:147], v[160:163], v[112:115], v[144:147]
	s_waitcnt lgkmcnt(0)
	v_mfma_f32_16x16x32_bf16 v[10:13], v[176:179], v[112:115], v[10:13]
	global_load_dwordx4 v[112:115], v[80:81], off
	s_waitcnt vmcnt(4)
	v_mfma_f32_16x16x32_bf16 v[104:107], v[160:163], v[148:151], v[104:107]
	v_mfma_f32_16x16x32_bf16 v[100:103], v[176:179], v[148:151], v[100:103]
	ds_read_b128 v[148:151], v137 offset:384
	v_mfma_f32_16x16x32_bf16 v[116:119], v[160:163], v[172:175], v[116:119]
	ds_read_b128 v[160:163], v137 offset:448
	v_mfma_f32_16x16x32_bf16 v[2:5], v[176:179], v[156:159], v[2:5]
	global_load_dwordx4 v[156:159], v[42:43], off offset:448
	v_mfma_f32_16x16x32_bf16 v[6:9], v[176:179], v[172:175], v[6:9]
	global_load_dwordx4 v[172:175], v[86:87], off
	s_waitcnt vmcnt(4) lgkmcnt(1)
	v_mfma_f32_16x16x32_bf16 v[108:111], v[148:151], v[152:155], v[108:111]
	s_waitcnt vmcnt(2)
	v_mfma_f32_16x16x32_bf16 v[116:119], v[148:151], v[112:115], v[116:119]
	v_mfma_f32_16x16x32_bf16 v[144:147], v[148:151], v[164:167], v[144:147]
	v_mfma_f32_16x16x32_bf16 v[104:107], v[148:151], v[168:171], v[104:107]
	ds_read_b128 v[148:151], v138 offset:384
	ds_read_b128 v[176:179], v138 offset:448
	s_waitcnt lgkmcnt(1)
	v_mfma_f32_16x16x32_bf16 v[2:5], v[148:151], v[152:155], v[2:5]
	v_mfma_f32_16x16x32_bf16 v[6:9], v[148:151], v[112:115], v[6:9]
	global_load_dwordx4 v[112:115], v[88:89], off
	v_mfma_f32_16x16x32_bf16 v[10:13], v[148:151], v[164:167], v[10:13]
	v_mfma_f32_16x16x32_bf16 v[100:103], v[148:151], v[168:171], v[100:103]
	global_load_dwordx4 v[148:151], v[90:91], off
	s_waitcnt lgkmcnt(0)
	s_barrier
; #define LAS __attribute__((address_space(3)))
; __device__ __forceinline__ void phase6(const Args& a, LAS unsigned char* lds, int tid, int lane, int wave, int vcu, int G) {
;     ...
;               for (int k8 = 0; k8 < 8; ++k8) { const int k0 = 256 * wave + 32 * k8 + 8 * l4;
; #pragma unroll
;                   for (int mt = 0; mt < 2; ++mt) { const bf16x8 ah = *(const LAS bf16x8*)(lds + RT_HI + (16 * mt + l15) * RT_ROWB + k0 * 2);
; #pragma unroll
;                       for (int et = 0; et < 4; ++et) acc[mt][et] = __builtin_amdgcn_mfma_f32_16x16x32_bf16(ah, bh[k8][et], acc[mt][et], 0, 0, 0); } }
;               __syncthreads();
; #pragma unroll
;               for (int mt = 0; mt < 2; ++mt)
; #pragma unroll
;                   for (int et = 0; et < 4; ++et)
; #pragma unroll
;                       for (int q = 0; q < 4; ++q) part[(wave * 32 + 16 * mt + 4 * l4 + q) * 64 + 16 * et + l15] = acc[mt][et][q]; }
;             __syncthreads();
; #pragma unroll
;             for (int q = 0; q < 4; ++q) { const int idx = tid + 512 * q; float sacc = 0.f;
; #pragma unroll
;                 for (int w = 0; w < 8; ++w) sacc += part[w * 2048 + idx];
;                 logit[idx] = sacc; }
;             __syncthreads();
	s_waitcnt vmcnt(3)
	v_mfma_f32_16x16x32_bf16 v[108:111], v[160:163], v[156:159], v[108:111]
	s_waitcnt vmcnt(2)
	v_mfma_f32_16x16x32_bf16 v[116:119], v[160:163], v[172:175], v[116:119]
	s_waitcnt vmcnt(1)
	v_mfma_f32_16x16x32_bf16 v[144:147], v[160:163], v[112:115], v[144:147]
	s_nop 5
	ds_write2_b32 v139, v108, v116 offset1:16
	ds_write2_b32 v139, v109, v117 offset0:64 offset1:80
	ds_write2_b32 v139, v110, v118 offset0:128 offset1:144
	ds_write2_b32 v139, v111, v119 offset0:192 offset1:208
	s_waitcnt vmcnt(0)
	v_mfma_f32_16x16x32_bf16 v[104:107], v[160:163], v[148:151], v[104:107]
	s_nop 7
	ds_write2_b32 v139, v144, v104 offset0:32 offset1:48
	ds_write2_b32 v139, v145, v105 offset0:96 offset1:112
	ds_write2_b32 v139, v146, v106 offset0:160 offset1:176
	v_mfma_f32_16x16x32_bf16 v[2:5], v[176:179], v[156:159], v[2:5]
	ds_write2_b32 v139, v147, v107 offset0:224 offset1:240
	v_mfma_f32_16x16x32_bf16 v[6:9], v[176:179], v[172:175], v[6:9]
	v_mfma_f32_16x16x32_bf16 v[10:13], v[176:179], v[112:115], v[10:13]
	s_nop 6
	ds_write2_b32 v16, v2, v6 offset1:16
	ds_write2_b32 v16, v3, v7 offset0:64 offset1:80
	ds_write2_b32 v16, v4, v8 offset0:128 offset1:144
	ds_write2_b32 v16, v5, v9 offset0:192 offset1:208
	v_mfma_f32_16x16x32_bf16 v[2:5], v[176:179], v[148:151], v[100:103]
	s_nop 7
	ds_write2_b32 v16, v10, v2 offset0:32 offset1:48
	ds_write2_b32 v16, v11, v3 offset0:96 offset1:112
	ds_write2_b32 v16, v12, v4 offset0:160 offset1:176
	ds_write2_b32 v16, v13, v5 offset0:224 offset1:240
	s_waitcnt lgkmcnt(0)
	s_barrier
	ds_read2st64_b32 v[2:3], v122 offset1:8
	ds_read2st64_b32 v[4:5], v122 offset0:32 offset1:40
	ds_read2st64_b32 v[6:7], v122 offset0:64 offset1:72
	ds_read2st64_b32 v[8:9], v122 offset0:96 offset1:104
	ds_read2st64_b32 v[10:11], v122 offset0:128 offset1:136
	ds_read2st64_b32 v[12:13], v122 offset0:160 offset1:168
	ds_read2st64_b32 v[100:101], v122 offset0:192 offset1:200
	ds_read2st64_b32 v[102:103], v122 offset0:224 offset1:232
	s_waitcnt lgkmcnt(7)
	v_add_f32_e32 v2, 0, v2
	s_waitcnt lgkmcnt(6)
	v_add_f32_e32 v2, v2, v4
	s_waitcnt lgkmcnt(5)
	v_add_f32_e32 v2, v2, v6
	s_waitcnt lgkmcnt(4)
	v_add_f32_e32 v2, v2, v8
	s_waitcnt lgkmcnt(3)
	v_add_f32_e32 v2, v2, v10
	s_waitcnt lgkmcnt(2)
	v_add_f32_e32 v2, v2, v12
	s_waitcnt lgkmcnt(1)
	v_add_f32_e32 v2, v2, v100
	s_waitcnt lgkmcnt(0)
	v_add_f32_e32 v2, v2, v102
	ds_write_b32 v123, v2
	v_add_f32_e32 v2, 0, v3
	v_add_f32_e32 v2, v2, v5
	v_add_f32_e32 v2, v2, v7
	v_add_f32_e32 v2, v2, v9
	v_add_f32_e32 v2, v2, v11
	v_add_f32_e32 v2, v2, v13
	v_add_f32_e32 v8, v2, v101
	ds_read2st64_b32 v[2:3], v122 offset0:16 offset1:24
	ds_read2st64_b32 v[4:5], v122 offset0:48 offset1:56
	ds_read2st64_b32 v[6:7], v122 offset0:80 offset1:88
	v_add_f32_e32 v8, v8, v103
	ds_write_b32 v124, v8
	s_waitcnt lgkmcnt(3)
	v_add_f32_e32 v2, 0, v2
	s_waitcnt lgkmcnt(2)
	v_add_f32_e32 v2, v2, v4
	s_waitcnt lgkmcnt(1)
	v_add_f32_e32 v2, v2, v6
	ds_read2st64_b32 v[8:9], v122 offset0:112 offset1:120
	ds_read2st64_b32 v[10:11], v122 offset0:144 offset1:152
	ds_read2st64_b32 v[12:13], v122 offset0:176 offset1:184
	ds_read2st64_b32 v[100:101], v122 offset0:208 offset1:216
	ds_read2st64_b32 v[102:103], v122 offset0:240 offset1:248
	s_waitcnt lgkmcnt(4)
	v_add_f32_e32 v2, v2, v8
	s_waitcnt lgkmcnt(3)
	v_add_f32_e32 v2, v2, v10
	s_waitcnt lgkmcnt(2)
	v_add_f32_e32 v2, v2, v12
	s_waitcnt lgkmcnt(1)
	v_add_f32_e32 v2, v2, v100
	s_waitcnt lgkmcnt(0)
	v_add_f32_e32 v2, v2, v102
	ds_write_b32 v125, v2
	v_add_f32_e32 v2, 0, v3
	v_add_f32_e32 v2, v2, v5
	v_add_f32_e32 v2, v2, v7
	v_add_f32_e32 v2, v2, v9
	v_add_f32_e32 v2, v2, v11
	v_add_f32_e32 v2, v2, v13
	v_add_f32_e32 v2, v2, v101
	v_add_f32_e32 v2, v2, v103
	ds_write_b32 v126, v2
	s_waitcnt lgkmcnt(0)
	s_barrier
	s_branch .LBB0_1090

; template <class Epi, class Sched, bool FP8 = false>
; __device__ __forceinline__ void gemm_phase(LAS unsigned char* lds, const int K, const Sched& S, const Epi& E) {
;     ...
;     if (!S.next(0, cur)) return;
;     __device__ __forceinline__ bool next(int i, U& u) const {
;         const int nt = tile[3 * NTILE_MAX]; const int L = i * G + c; if (L >= nt * 8) return false;
;         const int t = L >> 3; u.pn = L & 7; const int e = tile[t]; u.row0 = tile[NTILE_MAX + t]; u.nrows = tile[2 * NTILE_MAX + t];
;         u.A = ACT + (size_t)u.row0 * 512; u.B = W + ((size_t)e * 2048 + u.pn * 256) * 512; return true;
.LBB0_1371:
	s_cmp_gt_i32 s94, 10
	s_cselect_b64 s[0:1], -1, 0
	s_cmp_lt_i32 s95, 11
	s_cselect_b64 s[2:3], -1, 0
	s_or_b64 s[0:1], s[0:1], s[2:3]
	s_and_b64 vcc, exec, s[0:1]
	s_cbranch_vccnz .LBB0_1462
	v_mov_b32_e32 v1, v0
	s_movk_i32 s0, 0x100
	v_mov_b32_e32 v1, 0x39e72000
	global_load_dword v1, v1, s[92:93] offset:256
	s_add_u32 s4, s92, 0x30b00000
	s_addc_u32 s5, s93, 0
	s_add_u32 s21, s92, 0x1c00000
	s_addc_u32 s28, s93, 0
	s_add_u32 s29, s92, 0x39e70000
	s_addc_u32 s30, s93, 0
	s_add_u32 s6, s92, 0x39e72100
	s_addc_u32 s7, s93, 0
	v_readfirstlane_b32 s16, v0
	s_waitcnt vmcnt(0)
	v_readfirstlane_b32 s1, v1
	s_mov_b32 s98, s1
	s_lshl_b32 s1, s1, 3
	s_cmp_lt_i32 s71, s1
	s_cselect_b64 s[8:9], -1, 0
	s_cmp_ge_i32 s71, s1
	s_cbranch_scc1 .LBB0_1374
	s_ashr_i32 s2, s71, 3
	s_ashr_i32 s3, s2, 31
	s_and_b32 s54, s71, 7
	s_lshl_b64 s[2:3], s[2:3], 2
	s_add_u32 s2, s29, s2
	s_addc_u32 s3, s30, s3
	v_mov_b32_e32 v1, 0
	global_load_dword v2, v1, s[2:3]
	global_load_dword v198, v1, s[2:3] offset:2816
	v_mov_b32_e32 v1, 0x1000
	global_load_dword v1, v1, s[2:3] offset:1536
	s_lshl_b32 s1, s54, 17
	s_waitcnt vmcnt(0)
	v_readfirstlane_b32 s2, v2
	s_ashr_i32 s3, s2, 31
	s_lshl_b64 s[2:3], s[2:3], 20
	s_add_u32 s2, s21, s2
	v_ashrrev_i32_e32 v199, 31, v198
	s_addc_u32 s3, s28, s3
	v_lshlrev_b64 v[2:3], 9, v[198:199]
	s_add_u32 s2, s2, s1
	v_lshl_add_u64 v[220:221], s[4:5], 0, v[2:3]
	s_addc_u32 s3, s3, 0
	s_andn2_b64 vcc, exec, s[8:9]
	s_cbranch_vccz .LBB0_1375
	s_branch .LBB0_1412

; #define PG8_STAGE(bufoff, gbase, v0, v1) do { \
;         __builtin_amdgcn_global_load_lds((const unsigned*)((const char*)(gbase) + (v0)), (LAS unsigned*)(lds + (bufoff) + ldsw), 16, 0, 0); \
;         __builtin_amdgcn_global_load_lds((const unsigned*)((const char*)(gbase) + (v1)), (LAS unsigned*)(lds + (bufoff) + ldsw + 8192), 16, 0, 0); } while (0)
; #define PG8_WAIT_V(n) asm volatile("s_waitcnt vmcnt(" #n ")" ::: "memory")
; #define PG8_BAR __builtin_amdgcn_s_barrier()
; template <class Epi, class Sched, bool FP8 = false>
; __device__ __forceinline__ void gemm_phase(LAS unsigned char* lds, const int K, const Sched& S, const Epi& E) {
;     ...
;     PG8_STAGE(PG8_SB(0, 0), cB, voffB[0], voffB[1]); PG8_STAGE(PG8_SB(0, 1), cB + hstepB, voffB[0], voffB[1]); PG8_STAGE(PG8_SA(0, 0), cA, vA[0], vA[1]); PG8_STAGE(PG8_SA(0, 1), cA, vA[2], vA[3]);
;     if (wr == 1) PG8_BAR;
;     PG8_WAIT_V(2); PG8_BAR;
;     PG8_STAGE(PG8_SB(1, 0), cB + kstep, voffB[0], voffB[1]); PG8_STAGE(PG8_SA(1, 0), cA + kstep, vA[0], vA[1]); PG8_STAGE(PG8_SB(1, 1), cB + hstepB + kstep, voffB[0], voffB[1]);
;     PG8_WAIT_V(6); PG8_BAR;
;     __device__ __forceinline__ bool next(int i, U& u) const {
;         const int nt = tile[3 * NTILE_MAX]; const int L = i * G + c; if (L >= nt * 8) return false;
;         const int t = L >> 3; u.pn = L & 7; const int e = tile[t]; u.row0 = tile[NTILE_MAX + t]; u.nrows = tile[2 * NTILE_MAX + t];
;         u.A = ACT + (size_t)u.row0 * 512; u.B = W + ((size_t)e * 2048 + u.pn * 256) * 512; return true;
.LBB0_1377:
	s_add_u32 s12, s92, 0x9e00000
	s_mov_b64 s[14:15], 0x80
	s_addc_u32 s13, s93, 0
	v_lshl_add_u64 v[10:11], v[10:11], 0, s[14:15]
	s_add_i32 m0, s33, 0x18000
	s_waitcnt vmcnt(2)
	s_barrier
	global_load_lds_dwordx4 v[10:11], off
	v_lshl_add_u64 v[6:7], v[6:7], 0, s[14:15]
	s_add_i32 m0, s33, 0x1a000
	s_add_i32 s38, s33, 0x8000
	global_load_lds_dwordx4 v[6:7], off
	v_lshl_add_u64 v[6:7], v[8:9], 0, s[14:15]
	s_mov_b32 m0, s38
	s_add_i32 s39, s33, 0xa000
	global_load_lds_dwordx4 v[6:7], off
	v_lshl_add_u64 v[6:7], v[12:13], 0, s[14:15]
	s_mov_b32 m0, s39
	v_lshl_add_u64 v[4:5], v[4:5], 0, s[14:15]
	global_load_lds_dwordx4 v[6:7], off
	s_add_i32 m0, s33, 0x1c000
	v_lshl_add_u64 v[2:3], v[2:3], 0, s[14:15]
	global_load_lds_dwordx4 v[4:5], off
	s_add_i32 m0, s33, 0x1e000
	s_lshr_b32 s1, s1, 26
	global_load_lds_dwordx4 v[2:3], off
	v_lshlrev_b32_e32 v2, 6, v0
	s_add_i32 s1, s0, s1
	v_and_b32_e32 v3, 0x3c0, v2
	v_lshlrev_b32_e32 v5, 2, v0
	s_ashr_i32 s40, s1, 6
	v_or_b32_e32 v4, v3, v18
	s_lshl_b32 s1, s17, 13
	v_and_b32_e32 v5, 32, v5
	v_bitop3_b32 v3, v3, v5, v18 bitop3:0x36
	v_bitop3_b32 v4, s1, v4, v5 bitop3:0xf6
	v_and_b32_e32 v2, 0x6000, v2
	v_lshlrev_b32_e32 v5, 9, v16
	s_lshl_b32 s1, s18, 12
	v_or3_b32 v2, v14, v2, v5
	s_and_b32 s1, s1, 0x3000
	v_add_u32_e32 v2, v2, v15
	v_or_b32_e32 v199, s1, v3
	v_or_b32_e32 v2, 0x10000, v2
	v_mov_b32_e32 v3, v66
	v_lshl_add_u64 v[212:213], v[2:3], 0, s[14:15]
	v_add_u16_e32 v2, v14, v15
	s_cmp_gt_i32 s0, 63
	v_and_b32_e32 v2, 0xfe, v2
	s_cselect_b64 s[0:1], -1, 0
	s_add_i32 s41, s40, -2
	v_and_b32_e32 v2, 0xffff, v2
	v_lshlrev_b32_e32 v3, 2, v17
	s_mov_b32 s18, 0xe000
	s_cmpk_lt_u32 s16, 0x100
	v_and_or_b32 v2, v3, s18, v2
	s_waitcnt vmcnt(6)
	s_cselect_b64 s[16:17], -1, 0
	v_or3_b32 v2, v5, v2, s19
	v_mov_b32_e32 v3, v66
	s_add_i32 s45, 0, 0x10000
	s_add_i32 s47, 0, 0x14000
	v_lshl_add_u64 v[214:215], v[2:3], 0, s[14:15]
	v_cndmask_b32_e64 v2, 0, 1, s[0:1]
	v_add_u32_e32 v235, s45, v199
	v_add_u32_e32 v236, s47, v199
	s_add_i32 s45, s45, s31
	s_add_i32 s47, s47, s31
	v_mov_b32_e32 v209, v66
	v_mov_b32_e32 v211, v66
	v_mov_b32_e32 v234, 0x1000
	v_cmp_ne_u32_e64 s[0:1], 1, v2
	s_movk_i32 s42, 0x80
	s_mov_b64 s[18:19], 0x100
	v_add_u32_e32 v237, 0, v4
	s_add_i32 s43, s33, 0xc000
	s_add_i32 s44, s33, 0xe000
	s_add_i32 s46, s45, 0x2000
	s_add_i32 s48, s47, 0x2000
	s_add_i32 s49, 0, 0x18000
	s_brev_b32 s20, 60
	s_movk_i32 s50, 0xffc0
	s_mov_b32 s51, 0xc3e00000
	s_add_i32 s52, 0, 0x1c000
	v_mov_b32_e32 v238, 0x43e00000
	v_mov_b64_e32 v[218:219], v[220:221]
	s_mov_b64 s[22:23], s[2:3]
	s_barrier
	s_add_i32 s73, s97, s71
	s_ashr_i32 s73, s73, 3
	s_lshl_b32 s73, s73, 2
	s_add_u32 s74, s29, s73
	s_addc_u32 s75, s30, 0
	s_load_dword s76, s[74:75], 0x0
	s_load_dword s77, s[74:75], 0xb00
	s_load_dword s78, s[74:75], 0x1600
	s_branch .LBB0_1380

;     __device__ __forceinline__ void aoffs(const U& u, const int (&R)[2], const int (&C)[2], unsigned (&v)[4]) const { D.aoffs(u, R, C, v); }
; template <class Epi, class Sched, bool FP8 = false>
; __device__ __forceinline__ void gemm_phase(LAS unsigned char* lds, const int K, const Sched& S, const Epi& E) {
;     ...
;         const bool has_next = S.next(ui + 1, nxt);
;         const bool lo_only = S.lo_only(cur);
;         const char* nA = has_next ? nxt.A : cA; const char* nB = has_next ? nxt.B : cB;
;         if (has_next) S.aoffs(nxt, R, C, vN); else { vN[0] = vA[0]; vN[1] = vA[1]; vN[2] = vA[2]; vN[3] = vA[3]; }
;     __device__ __forceinline__ bool next(int i, U& u) const {
;         const int nt = tile[3 * NTILE_MAX]; const int L = i * G + c; if (L >= nt * 8) return false;
;         const int t = L >> 3; u.pn = L & 7; const int e = tile[t]; u.row0 = tile[NTILE_MAX + t]; u.nrows = tile[2 * NTILE_MAX + t];
;         u.A = ACT + (size_t)u.row0 * 512; u.B = W + ((size_t)e * 2048 + u.pn * 256) * 512; return true;
.LBB0_1380:
	s_add_i32 s37, s37, 1
	s_mul_i32 s26, s37, s97
	s_add_i32 s26, s26, s71
	s_lshl_b32 s27, s98, 3
	s_cmp_lt_i32 s26, s27
	s_cselect_b64 s[24:25], -1, 0
	s_waitcnt lgkmcnt(0)
	s_cmp_ge_i32 s26, s27
	s_cbranch_scc1 .LBB0_1382
	s_and_b32 s53, s26, 7
	v_mov_b32_e32 v216, s77
	v_mov_b32_e32 v239, s78
	s_lshl_b32 s26, s53, 17
	s_mov_b32 s22, s76
	s_ashr_i32 s23, s22, 31
	s_lshl_b64 s[22:23], s[22:23], 20
	s_add_u32 s22, s21, s22
	v_ashrrev_i32_e32 v217, 31, v216
	s_addc_u32 s23, s28, s23
	v_lshlrev_b64 v[2:3], 9, v[216:217]
	s_add_u32 s22, s22, s26
	v_lshl_add_u64 v[218:219], s[4:5], 0, v[2:3]
	s_addc_u32 s23, s23, 0

;     __device__ __forceinline__ bool next(int i, U& u) const {
;         const int nt = tile[3 * NTILE_MAX]; const int L = i * G + c; if (L >= nt * 8) return false;
;         const int t = L >> 3; u.pn = L & 7; const int e = tile[t]; u.row0 = tile[NTILE_MAX + t]; u.nrows = tile[2 * NTILE_MAX + t];
;     __device__ __forceinline__ void operator()(const f32x4 (&acc)[2][2][4][2], const MoeU& u, int wr, int wc, int fr, int fq) const {
;         const int c0 = u.pn * 256 + wc * 64 + 16 * fq; constexpr float sc = SC_O / (SC_W * SC_A);
; #pragma unroll
;         for (int ai = 0; ai < 2; ++ai)
; #pragma unroll
;             for (int m = 0; m < 4; ++m) { const int r = ai * 128 + wr * 64 + m * 16 + fr;
;                 if (r < u.nrows) { const f32x4 a0 = acc[ai][0][m][0] * sc, a1 = acc[ai][0][m][1] * sc, b0 = acc[ai][1][m][0] * sc, b1 = acc[ai][1][m][1] * sc;
;                     v4u o; o.x = pk4_fp8(a0[0], a0[1], a0[2], a0[3]); o.y = pk4_fp8(a1[0], a1[1], a1[2], a1[3]); o.z = pk4_fp8(b0[0], b0[1], b0[2], b0[3]); o.w = pk4_fp8(b1[0], b1[1], b1[2], b1[3]);
;                     __builtin_nontemporal_store(o, (v4u*)(so + (size_t)(u.row0 + r) * 2048 + c0)); } }
.LBB0_1392:
	s_add_i32 s73, s37, 1
	s_mul_i32 s73, s73, s97
	s_add_i32 s73, s73, s71
	s_ashr_i32 s73, s73, 3
	s_lshl_b32 s73, s73, 2
	s_add_u32 s74, s29, s73
	s_addc_u32 s75, s30, 0
	s_load_dword s76, s[74:75], 0x0
	s_load_dword s77, s[74:75], 0xb00
	s_load_dword s78, s[74:75], 0x1600
	v_mov_b32_e32 v67, v0
	s_nop 15
	s_nop 15
	s_nop 0
	v_and_b32_e32 v71, 15, v67
	v_and_b32_e32 v70, 0xf0, v67
	v_ashrrev_i32_e32 v67, 2, v67
	v_lshl_or_b32 v70, s54, 8, v70
	v_and_or_b32 v67, v67, s50, v71
	v_ashrrev_i32_e32 v71, 31, v70
	v_cmp_lt_i32_e32 vcc, v67, v1
	s_and_saveexec_b64 s[2:3], vcc
	s_cbranch_execz .LBB0_1394
	v_med3_f32 v73, v194, s51, v238
	v_med3_f32 v74, v195, s51, v238
	v_mov_b32_e32 v72, v66
	v_cvt_pk_fp8_f32 v72, v73, v74
	v_med3_f32 v74, v190, s51, v238
	v_med3_f32 v77, v191, s51, v238
	v_mov_b32_e32 v73, v66
	v_cvt_pk_fp8_f32 v73, v74, v77
	v_med3_f32 v75, v196, s51, v238
	v_med3_f32 v76, v197, s51, v238
	v_cvt_pk_fp8_f32 v72, v75, v76 op_sel:[0,0,1]
	v_med3_f32 v74, v192, s51, v238
	v_med3_f32 v75, v193, s51, v238
	v_cvt_pk_fp8_f32 v73, v74, v75 op_sel:[0,0,1]
	v_med3_f32 v75, v226, s51, v238
	v_med3_f32 v76, v227, s51, v238
	v_mov_b32_e32 v74, v66
	v_cvt_pk_fp8_f32 v74, v75, v76
	v_med3_f32 v76, v228, s51, v238
	v_med3_f32 v79, v229, s51, v238
	v_mov_b32_e32 v75, v66
	v_cvt_pk_fp8_f32 v75, v76, v79
	v_med3_f32 v77, v224, s51, v238
	v_med3_f32 v78, v225, s51, v238
	v_cvt_pk_fp8_f32 v74, v77, v78 op_sel:[0,0,1]
	v_med3_f32 v76, v222, s51, v238
	v_med3_f32 v77, v223, s51, v238
	v_cvt_pk_fp8_f32 v75, v76, v77 op_sel:[0,0,1]
	v_add_u32_e32 v76, v67, v198
	v_ashrrev_i32_e32 v77, 31, v76
	v_lshlrev_b64 v[76:77], 11, v[76:77]
	v_lshl_add_u64 v[76:77], s[12:13], 0, v[76:77]
	v_lshl_add_u64 v[76:77], v[76:77], 0, v[70:71]
	global_store_dwordx4 v[76:77], v[72:75], off nt

	.amdhsa_kernel _Z3fwd4Args
		.amdhsa_group_segment_fixed_size 16384
		.amdhsa_private_segment_fixed_size 0
		.amdhsa_kernarg_size 496
		.amdhsa_user_sgpr_count 2
		.amdhsa_user_sgpr_dispatch_ptr 0
		.amdhsa_user_sgpr_queue_ptr 0
		.amdhsa_user_sgpr_kernarg_segment_ptr 1
		.amdhsa_user_sgpr_dispatch_id 0
		.amdhsa_user_sgpr_kernarg_preload_length 0
		.amdhsa_user_sgpr_kernarg_preload_offset 0
		.amdhsa_user_sgpr_private_segment_size 0
		.amdhsa_uses_dynamic_stack 0
		.amdhsa_enable_private_segment 0
		.amdhsa_system_sgpr_workgroup_id_x 1
		.amdhsa_system_sgpr_workgroup_id_y 0
		.amdhsa_system_sgpr_workgroup_id_z 0
		.amdhsa_system_sgpr_workgroup_info 0
		.amdhsa_system_vgpr_workitem_id 0
		.amdhsa_next_free_vgpr 247
		.amdhsa_next_free_sgpr 102
		.amdhsa_accum_offset 248
		.amdhsa_reserve_vcc 1
		.amdhsa_float_round_mode_32 0
		.amdhsa_float_round_mode_16_64 0
		.amdhsa_float_denorm_mode_32 3
		.amdhsa_float_denorm_mode_16_64 3
		.amdhsa_dx10_clamp 1
		.amdhsa_ieee_mode 1
		.amdhsa_fp16_overflow 0
		.amdhsa_tg_split 0
		.amdhsa_exception_fp_ieee_invalid_op 0
		.amdhsa_exception_fp_denorm_src 0
		.amdhsa_exception_fp_ieee_div_zero 0
		.amdhsa_exception_fp_ieee_overflow 0
		.amdhsa_exception_fp_ieee_underflow 0
		.amdhsa_exception_fp_ieee_inexact 0
		.amdhsa_exception_int_div_zero 0
	.end_amdhsa_kernel

; #define LAS __attribute__((address_space(3)))
; __global__ void __launch_bounds__(512, 2) fwd(Args args) {
;     extern __shared__ __attribute__((aligned(16))) unsigned char lds_raw[];
;     LAS unsigned char* lds = (LAS unsigned char*)lds_raw;
amdhsa.kernels:
  - .agpr_count:     0
    .args:
      - .offset:         0
        .size:           240
        .value_kind:     by_value
      - .offset:         240
        .size:           4
        .value_kind:     hidden_block_count_x
      - .offset:         244
        .size:           4
        .value_kind:     hidden_block_count_y
      - .offset:         248
        .size:           4
        .value_kind:     hidden_block_count_z
      - .offset:         252
        .size:           2
        .value_kind:     hidden_group_size_x
      - .offset:         254
        .size:           2
        .value_kind:     hidden_group_size_y
      - .offset:         256
        .size:           2
        .value_kind:     hidden_group_size_z
      - .offset:         258
        .size:           2
        .value_kind:     hidden_remainder_x
      - .offset:         260
        .size:           2
        .value_kind:     hidden_remainder_y
      - .offset:         262
        .size:           2
        .value_kind:     hidden_remainder_z
      - .offset:         280
        .size:           8
        .value_kind:     hidden_global_offset_x
      - .offset:         288
        .size:           8
        .value_kind:     hidden_global_offset_y
      - .offset:         296
        .size:           8
        .value_kind:     hidden_global_offset_z
      - .offset:         304
        .size:           2
        .value_kind:     hidden_grid_dims
      - .offset:         360
        .size:           4
        .value_kind:     hidden_dynamic_lds_size
    .group_segment_fixed_size: 16384
    .kernarg_segment_align: 8
    .kernarg_segment_size: 496
    .language:       OpenCL C
    .language_version:
      - 2
      - 0
    .max_flat_workgroup_size: 512
    .name:           _Z3fwd4Args
    .private_segment_fixed_size: 0
    .sgpr_count:     108
    .sgpr_spill_count: 61
    .symbol:         _Z3fwd4Args.kd
    .uniform_work_group_size: 1
    .uses_dynamic_stack: false
    .vgpr_count:     247
    .vgpr_spill_count: 0
    .wavefront_size: 64
